# stack13 plus removal of 16 pad s_nop 0 before PV MFMAs in the attention loops
# speedup vs baseline: 1.0090x; 1.0008x over previous
; #define AT_SBAR() __builtin_amdgcn_sched_barrier(0)
; template <int D0> DI void pv_one(f32x16& od, int vb, bf16x8 pa0, bf16x8 pa1, bf16x8 pa2, bf16x8 pa3) {
;     const s16x4 l0 = tr_read<v_rd_off(D0, 0, 0)>(vb), h0 = tr_read<v_rd_off(D0, 0, 1)>(vb), l1 = tr_read<v_rd_off(D0, 1, 0)>(vb), h1 = tr_read<v_rd_off(D0, 1, 1)>(vb);
;     const s16x4 l2 = tr_read<v_rd_off(D0, 2, 0)>(vb), h2 = tr_read<v_rd_off(D0, 2, 1)>(vb), l3 = tr_read<v_rd_off(D0, 3, 0)>(vb), h3 = tr_read<v_rd_off(D0, 3, 1)>(vb);
;     asm volatile("s_waitcnt lgkmcnt(0)" ::: "memory"); AT_SBAR();
;     ...
;     od = __builtin_amdgcn_mfma_f32_32x32x16_bf16(AT_PK(l0, h0), pa0, od, 0, 0, 0);
;     od = __builtin_amdgcn_mfma_f32_32x32x16_bf16(AT_PK(l1, h1), pa1, od, 0, 0, 0);
;     od = __builtin_amdgcn_mfma_f32_32x32x16_bf16(AT_PK(l2, h2), pa2, od, 0, 0, 0);
;     od = __builtin_amdgcn_mfma_f32_32x32x16_bf16(AT_PK(l3, h3), pa3, od, 0, 0, 0);
;     ...
; }
; DI void pv_all_sm(f32x16* o, int vb, bf16x8 pa0, bf16x8 pa1, bf16x8 pa2, bf16x8 pa3, f32x16& p0, f32x16& p1, float& m_ref, f32x16& negm, float& alpha) {
;     pv_one<0>(o[0], vb, pa0, pa1, pa2, pa3);
;     float pmax = p0[0];
; #pragma unroll
;     for (int r = 1; r < 16; ++r) pmax = fmaxf(pmax, p0[r]);
;     pv_one<1>(o[1], vb, pa0, pa1, pa2, pa3);
; #pragma unroll
;     for (int r = 0; r < 16; ++r) pmax = fmaxf(pmax, p1[r]);
;     { auto rr = __builtin_amdgcn_permlane32_swap(__float_as_uint(pmax), __float_as_uint(pmax), false, false); pmax = fmaxf(__uint_as_float(rr[0]), __uint_as_float(rr[1])); }
;     pv_one<2>(o[2], vb, pa0, pa1, pa2, pa3);
;     alpha = 1.f;
;     if (__builtin_expect(!__all(pmax <= THRL), 0)) {
;         const float dl = fmaxf(pmax, 0.f); m_ref += dl; alpha = __builtin_amdgcn_exp2f(-dl);
; #pragma unroll
;         for (int r = 0; r < 16; ++r) { p0[r] -= dl; p1[r] -= dl; }
; #pragma unroll
;         for (int r = 0; r < 16; ++r) negm[r] = -m_ref;
;     }
;     pv_one<3>(o[3], vb, pa0, pa1, pa2, pa3);
; #pragma unroll
;     for (int r = 0; r < 16; ++r) p0[r] = __builtin_amdgcn_exp2f(p0[r]);
; }
; DI void attn_pass(const Frame& F, CvRide& cv, const bf16_t* __restrict__ Qb, const bf16_t* __restrict__ Kh, const bf16_t* __restrict__ Vh, char* lds, f32x16 (&o)[4], float& l_out, const int wave_s) {
;     ...
;     const unsigned cv_ldo = (unsigned)(((tid >> 4) * 2 * 2048 + (tid & 15) * 4) * 4), cv_sto = (unsigned)((tid >> 3) * 2048 + 8 * (tid & 7));
.LBB4_704:
	s_lshl_b32 s67, s65, 14
	v_add_u32_e32 v186, s67, v253
	ds_read_b64_tr_b16 v[64:65], v186 offset:0
	ds_read_b64_tr_b16 v[66:67], v186 offset:0x100
	ds_read_b64_tr_b16 v[68:69], v186 offset:0x1000
	ds_read_b64_tr_b16 v[70:71], v186 offset:0x1100
	ds_read_b64_tr_b16 v[72:73], v186 offset:0x2000
	ds_read_b64_tr_b16 v[74:75], v186 offset:0x2100
	ds_read_b64_tr_b16 v[76:77], v186 offset:0x3000
	ds_read_b64_tr_b16 v[78:79], v186 offset:0x3100
	s_waitcnt lgkmcnt(0)
	v_mfma_f32_32x32x16_bf16 v[32:47], v[64:67], v[96:99], v[32:47]
	v_max_f32_e32 v64, v128, v129
	v_max3_f32 v64, v64, v130, v131
	v_max3_f32 v64, v64, v132, v133
	v_max3_f32 v64, v64, v134, v135
	v_max3_f32 v64, v64, v136, v137
	v_mfma_f32_32x32x16_bf16 v[32:47], v[68:71], v[108:111], v[32:47]
	v_max3_f32 v64, v64, v138, v139
	v_max3_f32 v66, v64, v140, v141
	ds_read_b64_tr_b16 v[64:65], v186 offset:0x200
	v_max3_f32 v180, v66, v142, v143
	ds_read_b64_tr_b16 v[66:67], v186 offset:0x300
	ds_read_b64_tr_b16 v[68:69], v186 offset:0x1200
	ds_read_b64_tr_b16 v[70:71], v186 offset:0x1300
	v_mfma_f32_32x32x16_bf16 v[32:47], v[72:75], v[100:103], v[32:47]
	ds_read_b64_tr_b16 v[72:73], v186 offset:0x2200
	ds_read_b64_tr_b16 v[74:75], v186 offset:0x2300
	ds_read_b64_tr_b16 v[214:215], v186 offset:0x3200
	ds_read_b64_tr_b16 v[216:217], v186 offset:0x3300
	v_mfma_f32_32x32x16_bf16 v[32:47], v[76:79], v[104:107], v[32:47]
	s_waitcnt lgkmcnt(0)
	v_mfma_f32_32x32x16_bf16 v[48:63], v[64:67], v[96:99], v[48:63]
	v_max3_f32 v76, v180, v112, v113
	v_max3_f32 v64, v76, v114, v115
	ds_read_b64_tr_b16 v[66:67], v186 offset:0x400
	v_max3_f32 v64, v64, v116, v117
	v_max3_f32 v64, v64, v118, v119
	v_max3_f32 v64, v64, v120, v121
	v_max3_f32 v64, v64, v122, v123
	v_mfma_f32_32x32x16_bf16 v[48:63], v[68:71], v[108:111], v[48:63]
	ds_read_b64_tr_b16 v[68:69], v186 offset:0x500
	ds_read_b64_tr_b16 v[70:71], v186 offset:0x1400
	v_max3_f32 v64, v64, v124, v125
	v_max3_f32 v64, v64, v126, v127
	v_mov_b32_e32 v65, v64
	s_nop 1
	v_permlane32_swap_b32_e32 v64, v65
	v_mfma_f32_32x32x16_bf16 v[48:63], v[72:75], v[100:103], v[48:63]
	ds_read_b64_tr_b16 v[72:73], v186 offset:0x1500
	ds_read_b64_tr_b16 v[74:75], v186 offset:0x2400
	ds_read_b64_tr_b16 v[76:77], v186 offset:0x2500
	ds_read_b64_tr_b16 v[218:219], v186 offset:0x3400
	ds_read_b64_tr_b16 v[220:221], v186 offset:0x3500
	v_mfma_f32_32x32x16_bf16 v[48:63], v[214:217], v[104:107], v[48:63]
	s_waitcnt lgkmcnt(0)
	v_max_f32_e32 v64, v64, v65
	v_mfma_f32_32x32x16_bf16 v[16:31], v[66:69], v[96:99], v[16:31]
	v_cmp_ge_f32_e32 vcc, s25, v64
	s_cmp_eq_u64 vcc, exec
	v_mfma_f32_32x32x16_bf16 v[16:31], v[70:73], v[108:111], v[16:31]
	v_mfma_f32_32x32x16_bf16 v[16:31], v[74:77], v[100:103], v[16:31]
	v_mfma_f32_32x32x16_bf16 v[16:31], v[218:221], v[104:107], v[16:31]
	s_cbranch_scc0 .LBB4_737
	v_mov_b32_e32 v180, 1.0
.LBB4_706:
	ds_read_b64_tr_b16 v[214:215], v186 offset:0x600
	ds_read_b64_tr_b16 v[216:217], v186 offset:0x700
	ds_read_b64_tr_b16 v[218:219], v186 offset:0x1600
	ds_read_b64_tr_b16 v[220:221], v186 offset:0x1700
	ds_read_b64_tr_b16 v[222:223], v186 offset:0x2600
	ds_read_b64_tr_b16 v[224:225], v186 offset:0x2700
	ds_read_b64_tr_b16 v[226:227], v186 offset:0x3600
	ds_read_b64_tr_b16 v[228:229], v186 offset:0x3700
	s_waitcnt lgkmcnt(0)
	v_mfma_f32_32x32x16_bf16 v[0:15], v[214:217], v[96:99], v[0:15]
	s_lshl_b32 s2, s64, 14
	s_add_i32 s2, s2, 0
	s_lshl_b32 s3, s64, 13
	v_add_u32_e32 v96, s2, v200
	s_sub_i32 s78, s2, s3
	s_waitcnt vmcnt(0)
	v_add_u32_e32 v97, s2, v201
	v_mfma_f32_32x32x16_bf16 v[0:15], v[218:221], v[108:111], v[0:15]
	ds_write_b128 v96, v[176:179]
	v_add_u32_e32 v96, s78, v202
	ds_write_b128 v97, v[172:175]
	ds_write_b128 v96, v[168:171] offset:49152
	s_andn2_b64 s[2:3], exec, s[34:35]
	s_andn2_b64 vcc, exec, s[34:35]
	v_mfma_f32_32x32x16_bf16 v[0:15], v[222:225], v[100:103], v[0:15]
	v_mfma_f32_32x32x16_bf16 v[0:15], v[226:229], v[104:107], v[0:15]
	s_cbranch_vccnz .LBB4_711
	v_med3_f32 v97, v160, -v255, v255
	v_med3_f32 v98, v164, -v255, v255
	v_cvt_scalef32_pk_fp8_f32 v99, v97, v98, s93
	v_med3_f32 v97, v161, -v255, v255
	v_med3_f32 v98, v165, -v255, v255
	v_cvt_scalef32_pk_fp8_f32 v100, v97, v98, s93
	v_med3_f32 v97, v162, -v255, v255
	v_med3_f32 v98, v166, -v255, v255
	s_bitcmp1_b32 s58, 0
	v_cvt_scalef32_pk_fp8_f32 v101, v97, v98, s93
	s_cselect_b32 s8, 0x1100, 0
	v_med3_f32 v97, v163, -v255, v255
	v_med3_f32 v98, v167, -v255, v255
	v_cmp_eq_u32_e32 vcc, 0, v181
	v_add_u32_e32 v96, s8, v191
	v_cvt_scalef32_pk_fp8_f32 v102, v97, v98, s93
	s_and_b64 vcc, exec, vcc
	s_and_b32 s34, s58, 31
	ds_write_b16 v96, v99
	ds_write_b16 v96, v100 offset:68
	ds_write_b16 v96, v101 offset:136
	ds_write_b16 v96, v102 offset:204
	s_cbranch_vccnz .LBB4_735
	s_lshl_b32 s8, s34, 7
	s_lshl_b32 s9, s58, 6
	s_and_b32 s8, s8, 0xf00
	s_and_b32 s9, s9, 64
	s_or_b32 s26, s8, s9
	s_cbranch_execnz .LBB4_710

; #define AT_SBAR() __builtin_amdgcn_sched_barrier(0)
; template <int D0> DI void pv_one(f32x16& od, int vb, bf16x8 pa0, bf16x8 pa1, bf16x8 pa2, bf16x8 pa3) {
;     const s16x4 l0 = tr_read<v_rd_off(D0, 0, 0)>(vb), h0 = tr_read<v_rd_off(D0, 0, 1)>(vb), l1 = tr_read<v_rd_off(D0, 1, 0)>(vb), h1 = tr_read<v_rd_off(D0, 1, 1)>(vb);
;     const s16x4 l2 = tr_read<v_rd_off(D0, 2, 0)>(vb), h2 = tr_read<v_rd_off(D0, 2, 1)>(vb), l3 = tr_read<v_rd_off(D0, 3, 0)>(vb), h3 = tr_read<v_rd_off(D0, 3, 1)>(vb);
;     asm volatile("s_waitcnt lgkmcnt(0)" ::: "memory"); AT_SBAR();
;     ...
;     od = __builtin_amdgcn_mfma_f32_32x32x16_bf16(AT_PK(l0, h0), pa0, od, 0, 0, 0);
;     od = __builtin_amdgcn_mfma_f32_32x32x16_bf16(AT_PK(l1, h1), pa1, od, 0, 0, 0);
;     od = __builtin_amdgcn_mfma_f32_32x32x16_bf16(AT_PK(l2, h2), pa2, od, 0, 0, 0);
;     od = __builtin_amdgcn_mfma_f32_32x32x16_bf16(AT_PK(l3, h3), pa3, od, 0, 0, 0);
;     ...
; }
; DI void pv_all_sm(f32x16* o, int vb, bf16x8 pa0, bf16x8 pa1, bf16x8 pa2, bf16x8 pa3, f32x16& p0, f32x16& p1, float& m_ref, f32x16& negm, float& alpha) {
;     pv_one<0>(o[0], vb, pa0, pa1, pa2, pa3);
;     float pmax = p0[0];
; #pragma unroll
;     for (int r = 1; r < 16; ++r) pmax = fmaxf(pmax, p0[r]);
;     pv_one<1>(o[1], vb, pa0, pa1, pa2, pa3);
; #pragma unroll
;     for (int r = 0; r < 16; ++r) pmax = fmaxf(pmax, p1[r]);
;     { auto rr = __builtin_amdgcn_permlane32_swap(__float_as_uint(pmax), __float_as_uint(pmax), false, false); pmax = fmaxf(__uint_as_float(rr[0]), __uint_as_float(rr[1])); }
;     pv_one<2>(o[2], vb, pa0, pa1, pa2, pa3);
;     alpha = 1.f;
;     if (__builtin_expect(!__all(pmax <= THRL), 0)) {
;         const float dl = fmaxf(pmax, 0.f); m_ref += dl; alpha = __builtin_amdgcn_exp2f(-dl);
; #pragma unroll
;         for (int r = 0; r < 16; ++r) { p0[r] -= dl; p1[r] -= dl; }
; #pragma unroll
;         for (int r = 0; r < 16; ++r) negm[r] = -m_ref;
;     }
;     pv_one<3>(o[3], vb, pa0, pa1, pa2, pa3);
; #pragma unroll
;     for (int r = 0; r < 16; ++r) p0[r] = __builtin_amdgcn_exp2f(p0[r]);
; }
; DI void attn_pass(const Frame& F, CvRide& cv, const bf16_t* __restrict__ Qb, const bf16_t* __restrict__ Kh, const bf16_t* __restrict__ Vh, char* lds, f32x16 (&o)[4], float& l_out, const int wave_s) {
;     ...
;     const unsigned cv_ldo = (unsigned)(((tid >> 4) * 2 * 2048 + (tid & 15) * 4) * 4), cv_sto = (unsigned)((tid >> 3) * 2048 + 8 * (tid & 7));
.LBB4_725:
	v_lshl_add_u32 v215, s66, 14, v253
	ds_read_b64_tr_b16 v[216:217], v215 offset:0
	ds_read_b64_tr_b16 v[218:219], v215 offset:0x100
	ds_read_b64_tr_b16 v[220:221], v215 offset:0x1000
	ds_read_b64_tr_b16 v[222:223], v215 offset:0x1100
	ds_read_b64_tr_b16 v[224:225], v215 offset:0x2000
	ds_read_b64_tr_b16 v[226:227], v215 offset:0x2100
	ds_read_b64_tr_b16 v[228:229], v215 offset:0x3000
	ds_read_b64_tr_b16 v[230:231], v215 offset:0x3100
	s_waitcnt lgkmcnt(0)
	v_mfma_f32_32x32x16_bf16 v[32:47], v[216:219], v[120:123], v[32:47]
	v_max_f32_e32 v186, v128, v129
	ds_read_b64_tr_b16 v[216:217], v215 offset:0x200
	ds_read_b64_tr_b16 v[218:219], v215 offset:0x300
	v_max3_f32 v186, v186, v130, v131
	v_max3_f32 v186, v186, v132, v133
	v_mfma_f32_32x32x16_bf16 v[32:47], v[220:223], v[124:127], v[32:47]
	ds_read_b64_tr_b16 v[220:221], v215 offset:0x1200
	ds_read_b64_tr_b16 v[222:223], v215 offset:0x1300
	v_max3_f32 v186, v186, v134, v135
	v_max3_f32 v186, v186, v136, v137
	v_max3_f32 v186, v186, v138, v139
	v_max3_f32 v186, v186, v140, v141
	v_max3_f32 v186, v186, v142, v143
	v_mfma_f32_32x32x16_bf16 v[32:47], v[224:227], v[112:115], v[32:47]
	ds_read_b64_tr_b16 v[224:225], v215 offset:0x2200
	ds_read_b64_tr_b16 v[226:227], v215 offset:0x2300
	ds_read_b64_tr_b16 v[232:233], v215 offset:0x3200
	ds_read_b64_tr_b16 v[234:235], v215 offset:0x3300
	v_mfma_f32_32x32x16_bf16 v[32:47], v[228:231], v[116:119], v[32:47]
	s_waitcnt lgkmcnt(0)
	v_mfma_f32_32x32x16_bf16 v[48:63], v[216:219], v[120:123], v[48:63]
	v_max3_f32 v186, v186, v96, v97
	v_max3_f32 v186, v186, v98, v99
	ds_read_b64_tr_b16 v[218:219], v215 offset:0x400
	v_max3_f32 v186, v186, v100, v101
	v_max3_f32 v186, v186, v102, v103
	v_max3_f32 v186, v186, v104, v105
	v_max3_f32 v186, v186, v106, v107
	v_mfma_f32_32x32x16_bf16 v[48:63], v[220:223], v[124:127], v[48:63]
	ds_read_b64_tr_b16 v[220:221], v215 offset:0x500
	ds_read_b64_tr_b16 v[222:223], v215 offset:0x1400
	v_max3_f32 v186, v186, v108, v109
	v_max3_f32 v186, v186, v110, v111
	v_mov_b32_e32 v216, v186
	s_nop 1
	v_permlane32_swap_b32_e32 v186, v216
	v_mfma_f32_32x32x16_bf16 v[48:63], v[224:227], v[112:115], v[48:63]
	ds_read_b64_tr_b16 v[224:225], v215 offset:0x1500
	ds_read_b64_tr_b16 v[226:227], v215 offset:0x2400
	ds_read_b64_tr_b16 v[228:229], v215 offset:0x2500
	ds_read_b64_tr_b16 v[236:237], v215 offset:0x3400
	ds_read_b64_tr_b16 v[238:239], v215 offset:0x3500
	v_mfma_f32_32x32x16_bf16 v[48:63], v[232:235], v[116:119], v[48:63]
	s_waitcnt lgkmcnt(0)
	v_max_f32_e32 v216, v186, v216
	v_mfma_f32_32x32x16_bf16 v[16:31], v[218:221], v[120:123], v[16:31]
	v_cmp_ge_f32_e32 vcc, s25, v216
	s_cmp_eq_u64 vcc, exec
	v_mov_b32_e32 v186, 1.0
	v_mfma_f32_32x32x16_bf16 v[16:31], v[222:225], v[124:127], v[16:31]
	v_mfma_f32_32x32x16_bf16 v[16:31], v[226:229], v[112:115], v[16:31]
	v_mfma_f32_32x32x16_bf16 v[16:31], v[236:239], v[116:119], v[16:31]
	s_cbranch_scc0 .LBB4_738
.LBB4_726:
	ds_read_b64_tr_b16 v[216:217], v215 offset:0x600
	ds_read_b64_tr_b16 v[218:219], v215 offset:0x700
	ds_read_b64_tr_b16 v[220:221], v215 offset:0x1600
	ds_read_b64_tr_b16 v[222:223], v215 offset:0x1700
	ds_read_b64_tr_b16 v[224:225], v215 offset:0x2600
	ds_read_b64_tr_b16 v[226:227], v215 offset:0x2700
	ds_read_b64_tr_b16 v[228:229], v215 offset:0x3600
	ds_read_b64_tr_b16 v[230:231], v215 offset:0x3700
	s_waitcnt lgkmcnt(0)
	v_mfma_f32_32x32x16_bf16 v[0:15], v[216:219], v[120:123], v[0:15]
	s_add_i32 s2, s67, 0
	v_add_u32_e32 v120, s2, v200
	s_waitcnt vmcnt(0)
	ds_write_b128 v120, v[176:179]
	s_mov_b32 s26, 0
	s_andn2_b64 vcc, exec, s[34:35]
	v_mfma_f32_32x32x16_bf16 v[0:15], v[220:223], v[124:127], v[0:15]
	v_mfma_f32_32x32x16_bf16 v[0:15], v[224:227], v[112:115], v[0:15]
	v_add_u32_e32 v112, s2, v201
	ds_write_b128 v112, v[172:175]
	v_lshl_add_u32 v112, s65, 13, v203
	ds_write_b128 v112, v[168:171] offset:49152
	s_andn2_b64 s[2:3], exec, s[34:35]
	v_mfma_f32_32x32x16_bf16 v[0:15], v[228:231], v[116:119], v[0:15]
	s_cbranch_vccnz .LBB4_731
	v_med3_f32 v113, v160, -v255, v255
	v_med3_f32 v114, v164, -v255, v255
	v_cvt_scalef32_pk_fp8_f32 v115, v113, v114, s93
	v_med3_f32 v113, v161, -v255, v255
	v_med3_f32 v114, v165, -v255, v255
	v_cvt_scalef32_pk_fp8_f32 v116, v113, v114, s93
	v_med3_f32 v113, v162, -v255, v255
	v_med3_f32 v114, v166, -v255, v255
	s_bitcmp1_b32 s58, 0
	v_cvt_scalef32_pk_fp8_f32 v117, v113, v114, s93
	s_cselect_b32 s8, 0x1100, 0
	v_med3_f32 v113, v163, -v255, v255
	v_med3_f32 v114, v167, -v255, v255
	v_cmp_eq_u32_e32 vcc, 0, v181
	v_add_u32_e32 v112, s8, v191
	v_cvt_scalef32_pk_fp8_f32 v118, v113, v114, s93
	s_and_b64 vcc, exec, vcc
	s_and_b32 s37, s58, 31
	ds_write_b16 v112, v115
	ds_write_b16 v112, v116 offset:68
	ds_write_b16 v112, v117 offset:136
	ds_write_b16 v112, v118 offset:204
	s_cbranch_vccnz .LBB4_736
	s_lshl_b32 s8, s37, 7
	s_lshl_b32 s9, s58, 6
	s_and_b32 s8, s8, 0xf00
	s_and_b32 s9, s9, 64
	s_or_b32 s26, s8, s9
	s_cbranch_execnz .LBB4_730

; #define AT_SBAR() __builtin_amdgcn_sched_barrier(0)
; template <int D0> DI void pv_one(f32x16& od, int vb, bf16x8 pa0, bf16x8 pa1, bf16x8 pa2, bf16x8 pa3) {
;     const s16x4 l0 = tr_read<v_rd_off(D0, 0, 0)>(vb), h0 = tr_read<v_rd_off(D0, 0, 1)>(vb), l1 = tr_read<v_rd_off(D0, 1, 0)>(vb), h1 = tr_read<v_rd_off(D0, 1, 1)>(vb);
;     const s16x4 l2 = tr_read<v_rd_off(D0, 2, 0)>(vb), h2 = tr_read<v_rd_off(D0, 2, 1)>(vb), l3 = tr_read<v_rd_off(D0, 3, 0)>(vb), h3 = tr_read<v_rd_off(D0, 3, 1)>(vb);
;     asm volatile("s_waitcnt lgkmcnt(0)" ::: "memory"); AT_SBAR();
;     ...
;     od = __builtin_amdgcn_mfma_f32_32x32x16_bf16(AT_PK(l0, h0), pa0, od, 0, 0, 0);
;     od = __builtin_amdgcn_mfma_f32_32x32x16_bf16(AT_PK(l1, h1), pa1, od, 0, 0, 0);
;     od = __builtin_amdgcn_mfma_f32_32x32x16_bf16(AT_PK(l2, h2), pa2, od, 0, 0, 0);
;     od = __builtin_amdgcn_mfma_f32_32x32x16_bf16(AT_PK(l3, h3), pa3, od, 0, 0, 0);
;     ...
; }
; DI void pv_all_sm(f32x16* o, int vb, bf16x8 pa0, bf16x8 pa1, bf16x8 pa2, bf16x8 pa3, f32x16& p0, f32x16& p1, float& m_ref, f32x16& negm, float& alpha) {
;     pv_one<0>(o[0], vb, pa0, pa1, pa2, pa3);
;     float pmax = p0[0];
; #pragma unroll
;     for (int r = 1; r < 16; ++r) pmax = fmaxf(pmax, p0[r]);
;     pv_one<1>(o[1], vb, pa0, pa1, pa2, pa3);
; #pragma unroll
;     for (int r = 0; r < 16; ++r) pmax = fmaxf(pmax, p1[r]);
;     { auto rr = __builtin_amdgcn_permlane32_swap(__float_as_uint(pmax), __float_as_uint(pmax), false, false); pmax = fmaxf(__uint_as_float(rr[0]), __uint_as_float(rr[1])); }
;     pv_one<2>(o[2], vb, pa0, pa1, pa2, pa3);
;     alpha = 1.f;
;     if (__builtin_expect(!__all(pmax <= THRL), 0)) {
;         const float dl = fmaxf(pmax, 0.f); m_ref += dl; alpha = __builtin_amdgcn_exp2f(-dl);
; #pragma unroll
;         for (int r = 0; r < 16; ++r) { p0[r] -= dl; p1[r] -= dl; }
; #pragma unroll
;         for (int r = 0; r < 16; ++r) negm[r] = -m_ref;
;     }
;     pv_one<3>(o[3], vb, pa0, pa1, pa2, pa3);
; #pragma unroll
;     for (int r = 0; r < 16; ++r) p0[r] = __builtin_amdgcn_exp2f(p0[r]);
; }
; DI void attn_pass(const Frame& F, CvRide& cv, const bf16_t* __restrict__ Qb, const bf16_t* __restrict__ Kh, const bf16_t* __restrict__ Vh, char* lds, f32x16 (&o)[4], float& l_out, const int wave_s) {
;     ...
;     const unsigned cv_ldo = (unsigned)(((tid >> 4) * 2 * 2048 + (tid & 15) * 4) * 4), cv_sto = (unsigned)((tid >> 3) * 2048 + 8 * (tid & 7));
.LBB4_777:
	s_lshl_b32 s31, s29, 14
	v_add_u32_e32 v182, s31, v253
	ds_read_b64_tr_b16 v[64:65], v182 offset:0
	ds_read_b64_tr_b16 v[66:67], v182 offset:0x100
	ds_read_b64_tr_b16 v[68:69], v182 offset:0x1000
	ds_read_b64_tr_b16 v[70:71], v182 offset:0x1100
	ds_read_b64_tr_b16 v[72:73], v182 offset:0x2000
	ds_read_b64_tr_b16 v[74:75], v182 offset:0x2100
	ds_read_b64_tr_b16 v[76:77], v182 offset:0x3000
	ds_read_b64_tr_b16 v[78:79], v182 offset:0x3100
	s_waitcnt lgkmcnt(0)
	v_mfma_f32_32x32x16_bf16 v[48:63], v[64:67], v[96:99], v[48:63]
	v_max_f32_e32 v64, v128, v129
	v_max3_f32 v64, v64, v130, v131
	v_max3_f32 v64, v64, v132, v133
	v_max3_f32 v64, v64, v134, v135
	v_max3_f32 v64, v64, v136, v137
	v_mfma_f32_32x32x16_bf16 v[48:63], v[68:71], v[108:111], v[48:63]
	v_max3_f32 v64, v64, v138, v139
	v_max3_f32 v66, v64, v140, v141
	ds_read_b64_tr_b16 v[64:65], v182 offset:0x200
	v_max3_f32 v180, v66, v142, v143
	ds_read_b64_tr_b16 v[66:67], v182 offset:0x300
	ds_read_b64_tr_b16 v[68:69], v182 offset:0x1200
	ds_read_b64_tr_b16 v[70:71], v182 offset:0x1300
	v_mfma_f32_32x32x16_bf16 v[48:63], v[72:75], v[100:103], v[48:63]
	ds_read_b64_tr_b16 v[72:73], v182 offset:0x2200
	ds_read_b64_tr_b16 v[74:75], v182 offset:0x2300
	ds_read_b64_tr_b16 v[218:219], v182 offset:0x3200
	ds_read_b64_tr_b16 v[220:221], v182 offset:0x3300
	v_mfma_f32_32x32x16_bf16 v[48:63], v[76:79], v[104:107], v[48:63]
	s_waitcnt lgkmcnt(0)
	v_mfma_f32_32x32x16_bf16 v[32:47], v[64:67], v[96:99], v[32:47]
	v_max3_f32 v76, v180, v112, v113
	v_max3_f32 v64, v76, v114, v115
	ds_read_b64_tr_b16 v[66:67], v182 offset:0x400
	v_max3_f32 v64, v64, v116, v117
	v_max3_f32 v64, v64, v118, v119
	v_max3_f32 v64, v64, v120, v121
	v_max3_f32 v64, v64, v122, v123
	v_mfma_f32_32x32x16_bf16 v[32:47], v[68:71], v[108:111], v[32:47]
	ds_read_b64_tr_b16 v[68:69], v182 offset:0x500
	ds_read_b64_tr_b16 v[70:71], v182 offset:0x1400
	v_max3_f32 v64, v64, v124, v125
	v_max3_f32 v64, v64, v126, v127
	v_mov_b32_e32 v65, v64
	s_nop 1
	v_permlane32_swap_b32_e32 v64, v65
	v_mfma_f32_32x32x16_bf16 v[32:47], v[72:75], v[100:103], v[32:47]
	ds_read_b64_tr_b16 v[72:73], v182 offset:0x1500
	ds_read_b64_tr_b16 v[74:75], v182 offset:0x2400
	ds_read_b64_tr_b16 v[76:77], v182 offset:0x2500
	ds_read_b64_tr_b16 v[222:223], v182 offset:0x3400
	ds_read_b64_tr_b16 v[224:225], v182 offset:0x3500
	v_mfma_f32_32x32x16_bf16 v[32:47], v[218:221], v[104:107], v[32:47]
	s_waitcnt lgkmcnt(0)
	v_max_f32_e32 v64, v64, v65
	v_mfma_f32_32x32x16_bf16 v[16:31], v[66:69], v[96:99], v[16:31]
	v_cmp_ge_f32_e32 vcc, s26, v64
	s_cmp_eq_u64 vcc, exec
	v_mfma_f32_32x32x16_bf16 v[16:31], v[70:73], v[108:111], v[16:31]
	v_mfma_f32_32x32x16_bf16 v[16:31], v[74:77], v[100:103], v[16:31]
	v_mfma_f32_32x32x16_bf16 v[16:31], v[222:225], v[104:107], v[16:31]
	s_cbranch_scc0 .LBB4_810
	v_mov_b32_e32 v180, 1.0
.LBB4_779:
	ds_read_b64_tr_b16 v[218:219], v182 offset:0x600
	ds_read_b64_tr_b16 v[220:221], v182 offset:0x700
	ds_read_b64_tr_b16 v[222:223], v182 offset:0x1600
	ds_read_b64_tr_b16 v[224:225], v182 offset:0x1700
	ds_read_b64_tr_b16 v[226:227], v182 offset:0x2600
	ds_read_b64_tr_b16 v[228:229], v182 offset:0x2700
	ds_read_b64_tr_b16 v[230:231], v182 offset:0x3600
	ds_read_b64_tr_b16 v[232:233], v182 offset:0x3700
	s_waitcnt lgkmcnt(0)
	v_mfma_f32_32x32x16_bf16 v[0:15], v[218:221], v[96:99], v[0:15]
	s_lshl_b32 s2, s15, 14
	s_add_i32 s2, s2, 0
	s_lshl_b32 s3, s15, 13
	v_add_u32_e32 v96, s2, v203
	s_sub_i32 s65, s2, s3
	s_waitcnt vmcnt(0)
	v_add_u32_e32 v97, s2, v204
	v_mfma_f32_32x32x16_bf16 v[0:15], v[222:225], v[108:111], v[0:15]
	ds_write_b128 v96, v[176:179]
	v_add_u32_e32 v96, s65, v205
	ds_write_b128 v97, v[172:175]
	ds_write_b128 v96, v[168:171] offset:49152
	s_andn2_b64 s[2:3], exec, s[22:23]
	s_andn2_b64 vcc, exec, s[22:23]
	v_mfma_f32_32x32x16_bf16 v[0:15], v[226:229], v[100:103], v[0:15]
	v_mfma_f32_32x32x16_bf16 v[0:15], v[230:233], v[104:107], v[0:15]
	s_cbranch_vccnz .LBB4_784
	v_med3_f32 v97, v160, -v255, v255
	v_med3_f32 v98, v164, -v255, v255
	v_cvt_scalef32_pk_fp8_f32 v99, v97, v98, s93
	v_med3_f32 v97, v161, -v255, v255
	v_med3_f32 v98, v165, -v255, v255
	v_cvt_scalef32_pk_fp8_f32 v100, v97, v98, s93
	v_med3_f32 v97, v162, -v255, v255
	v_med3_f32 v98, v166, -v255, v255
	s_bitcmp1_b32 s58, 0
	v_cvt_scalef32_pk_fp8_f32 v101, v97, v98, s93
	s_cselect_b32 s8, 0x1100, 0
	v_med3_f32 v97, v163, -v255, v255
	v_med3_f32 v98, v167, -v255, v255
	v_cmp_eq_u32_e32 vcc, 0, v181
	v_add_u32_e32 v96, s8, v195
	v_cvt_scalef32_pk_fp8_f32 v102, v97, v98, s93
	s_and_b64 vcc, exec, vcc
	s_and_b32 s22, s58, 31
	ds_write_b16 v96, v99
	ds_write_b16 v96, v100 offset:68
	ds_write_b16 v96, v101 offset:136
	ds_write_b16 v96, v102 offset:204
	s_cbranch_vccnz .LBB4_808
	s_lshl_b32 s8, s22, 7
	s_lshl_b32 s9, s58, 6
	s_and_b32 s8, s8, 0xf00
	s_and_b32 s9, s9, 64
	s_or_b32 s20, s8, s9
	s_cbranch_execnz .LBB4_783

; #define AT_SBAR() __builtin_amdgcn_sched_barrier(0)
; template <int D0> DI void pv_one(f32x16& od, int vb, bf16x8 pa0, bf16x8 pa1, bf16x8 pa2, bf16x8 pa3) {
;     const s16x4 l0 = tr_read<v_rd_off(D0, 0, 0)>(vb), h0 = tr_read<v_rd_off(D0, 0, 1)>(vb), l1 = tr_read<v_rd_off(D0, 1, 0)>(vb), h1 = tr_read<v_rd_off(D0, 1, 1)>(vb);
;     const s16x4 l2 = tr_read<v_rd_off(D0, 2, 0)>(vb), h2 = tr_read<v_rd_off(D0, 2, 1)>(vb), l3 = tr_read<v_rd_off(D0, 3, 0)>(vb), h3 = tr_read<v_rd_off(D0, 3, 1)>(vb);
;     asm volatile("s_waitcnt lgkmcnt(0)" ::: "memory"); AT_SBAR();
;     ...
;     od = __builtin_amdgcn_mfma_f32_32x32x16_bf16(AT_PK(l0, h0), pa0, od, 0, 0, 0);
;     od = __builtin_amdgcn_mfma_f32_32x32x16_bf16(AT_PK(l1, h1), pa1, od, 0, 0, 0);
;     od = __builtin_amdgcn_mfma_f32_32x32x16_bf16(AT_PK(l2, h2), pa2, od, 0, 0, 0);
;     od = __builtin_amdgcn_mfma_f32_32x32x16_bf16(AT_PK(l3, h3), pa3, od, 0, 0, 0);
;     ...
; }
; DI void pv_all_sm(f32x16* o, int vb, bf16x8 pa0, bf16x8 pa1, bf16x8 pa2, bf16x8 pa3, f32x16& p0, f32x16& p1, float& m_ref, f32x16& negm, float& alpha) {
;     pv_one<0>(o[0], vb, pa0, pa1, pa2, pa3);
;     float pmax = p0[0];
; #pragma unroll
;     for (int r = 1; r < 16; ++r) pmax = fmaxf(pmax, p0[r]);
;     pv_one<1>(o[1], vb, pa0, pa1, pa2, pa3);
; #pragma unroll
;     for (int r = 0; r < 16; ++r) pmax = fmaxf(pmax, p1[r]);
;     { auto rr = __builtin_amdgcn_permlane32_swap(__float_as_uint(pmax), __float_as_uint(pmax), false, false); pmax = fmaxf(__uint_as_float(rr[0]), __uint_as_float(rr[1])); }
;     pv_one<2>(o[2], vb, pa0, pa1, pa2, pa3);
;     alpha = 1.f;
;     if (__builtin_expect(!__all(pmax <= THRL), 0)) {
;         const float dl = fmaxf(pmax, 0.f); m_ref += dl; alpha = __builtin_amdgcn_exp2f(-dl);
; #pragma unroll
;         for (int r = 0; r < 16; ++r) { p0[r] -= dl; p1[r] -= dl; }
; #pragma unroll
;         for (int r = 0; r < 16; ++r) negm[r] = -m_ref;
;     }
;     pv_one<3>(o[3], vb, pa0, pa1, pa2, pa3);
; #pragma unroll
;     for (int r = 0; r < 16; ++r) p0[r] = __builtin_amdgcn_exp2f(p0[r]);
; }
; DI void attn_pass(const Frame& F, CvRide& cv, const bf16_t* __restrict__ Qb, const bf16_t* __restrict__ Kh, const bf16_t* __restrict__ Vh, char* lds, f32x16 (&o)[4], float& l_out, const int wave_s) {
;     ...
;     const unsigned cv_ldo = (unsigned)(((tid >> 4) * 2 * 2048 + (tid & 15) * 4) * 4), cv_sto = (unsigned)((tid >> 3) * 2048 + 8 * (tid & 7));
.LBB4_798:
	v_lshl_add_u32 v219, s30, 14, v253
	ds_read_b64_tr_b16 v[220:221], v219 offset:0
	ds_read_b64_tr_b16 v[222:223], v219 offset:0x100
	ds_read_b64_tr_b16 v[224:225], v219 offset:0x1000
	ds_read_b64_tr_b16 v[226:227], v219 offset:0x1100
	ds_read_b64_tr_b16 v[228:229], v219 offset:0x2000
	ds_read_b64_tr_b16 v[230:231], v219 offset:0x2100
	ds_read_b64_tr_b16 v[232:233], v219 offset:0x3000
	ds_read_b64_tr_b16 v[234:235], v219 offset:0x3100
	s_waitcnt lgkmcnt(0)
	v_mfma_f32_32x32x16_bf16 v[48:63], v[220:223], v[120:123], v[48:63]
	v_max_f32_e32 v182, v128, v129
	ds_read_b64_tr_b16 v[220:221], v219 offset:0x200
	ds_read_b64_tr_b16 v[222:223], v219 offset:0x300
	v_max3_f32 v182, v182, v130, v131
	v_max3_f32 v182, v182, v132, v133
	v_mfma_f32_32x32x16_bf16 v[48:63], v[224:227], v[124:127], v[48:63]
	ds_read_b64_tr_b16 v[224:225], v219 offset:0x1200
	ds_read_b64_tr_b16 v[226:227], v219 offset:0x1300
	v_max3_f32 v182, v182, v134, v135
	v_max3_f32 v182, v182, v136, v137
	v_max3_f32 v182, v182, v138, v139
	v_max3_f32 v182, v182, v140, v141
	v_max3_f32 v182, v182, v142, v143
	v_mfma_f32_32x32x16_bf16 v[48:63], v[228:231], v[112:115], v[48:63]
	ds_read_b64_tr_b16 v[228:229], v219 offset:0x2200
	ds_read_b64_tr_b16 v[230:231], v219 offset:0x2300
	ds_read_b64_tr_b16 v[236:237], v219 offset:0x3200
	ds_read_b64_tr_b16 v[238:239], v219 offset:0x3300
	v_mfma_f32_32x32x16_bf16 v[48:63], v[232:235], v[116:119], v[48:63]
	s_waitcnt lgkmcnt(0)
	v_mfma_f32_32x32x16_bf16 v[32:47], v[220:223], v[120:123], v[32:47]
	v_max3_f32 v182, v182, v96, v97
	v_max3_f32 v182, v182, v98, v99
	ds_read_b64_tr_b16 v[222:223], v219 offset:0x400
	v_max3_f32 v182, v182, v100, v101
	v_max3_f32 v182, v182, v102, v103
	v_max3_f32 v182, v182, v104, v105
	v_max3_f32 v182, v182, v106, v107
	v_mfma_f32_32x32x16_bf16 v[32:47], v[224:227], v[124:127], v[32:47]
	ds_read_b64_tr_b16 v[224:225], v219 offset:0x500
	ds_read_b64_tr_b16 v[226:227], v219 offset:0x1400
	v_max3_f32 v182, v182, v108, v109
	v_max3_f32 v182, v182, v110, v111
	v_mov_b32_e32 v220, v182
	s_nop 1
	v_permlane32_swap_b32_e32 v182, v220
	v_mfma_f32_32x32x16_bf16 v[32:47], v[228:231], v[112:115], v[32:47]
	ds_read_b64_tr_b16 v[228:229], v219 offset:0x1500
	ds_read_b64_tr_b16 v[230:231], v219 offset:0x2400
	ds_read_b64_tr_b16 v[232:233], v219 offset:0x2500
	ds_read_b64_tr_b16 v[240:241], v219 offset:0x3400
	ds_read_b64_tr_b16 v[242:243], v219 offset:0x3500
	v_mfma_f32_32x32x16_bf16 v[32:47], v[236:239], v[116:119], v[32:47]
	s_waitcnt lgkmcnt(0)
	v_max_f32_e32 v220, v182, v220
	v_mfma_f32_32x32x16_bf16 v[16:31], v[222:225], v[120:123], v[16:31]
	v_cmp_ge_f32_e32 vcc, s26, v220
	s_cmp_eq_u64 vcc, exec
	v_mov_b32_e32 v182, 1.0
	v_mfma_f32_32x32x16_bf16 v[16:31], v[226:229], v[124:127], v[16:31]
	v_mfma_f32_32x32x16_bf16 v[16:31], v[230:233], v[112:115], v[16:31]
	v_mfma_f32_32x32x16_bf16 v[16:31], v[240:243], v[116:119], v[16:31]
	s_cbranch_scc0 .LBB4_811
.LBB4_799:
	ds_read_b64_tr_b16 v[220:221], v219 offset:0x600
	ds_read_b64_tr_b16 v[222:223], v219 offset:0x700
	ds_read_b64_tr_b16 v[224:225], v219 offset:0x1600
	ds_read_b64_tr_b16 v[226:227], v219 offset:0x1700
	ds_read_b64_tr_b16 v[228:229], v219 offset:0x2600
	ds_read_b64_tr_b16 v[230:231], v219 offset:0x2700
	ds_read_b64_tr_b16 v[232:233], v219 offset:0x3600
	ds_read_b64_tr_b16 v[234:235], v219 offset:0x3700
	s_waitcnt lgkmcnt(0)
	v_mfma_f32_32x32x16_bf16 v[0:15], v[220:223], v[120:123], v[0:15]
	s_add_i32 s2, s31, 0
	v_add_u32_e32 v120, s2, v203
	s_waitcnt vmcnt(0)
	ds_write_b128 v120, v[176:179]
	s_mov_b32 s20, 0
	s_andn2_b64 vcc, exec, s[22:23]
	v_mfma_f32_32x32x16_bf16 v[0:15], v[224:227], v[124:127], v[0:15]
	v_mfma_f32_32x32x16_bf16 v[0:15], v[228:231], v[112:115], v[0:15]
	v_add_u32_e32 v112, s2, v204
	ds_write_b128 v112, v[172:175]
	v_lshl_add_u32 v112, s29, 13, v206
	ds_write_b128 v112, v[168:171] offset:49152
	s_andn2_b64 s[2:3], exec, s[22:23]
	v_mfma_f32_32x32x16_bf16 v[0:15], v[232:235], v[116:119], v[0:15]
	s_cbranch_vccnz .LBB4_804
	v_med3_f32 v113, v160, -v255, v255
	v_med3_f32 v114, v164, -v255, v255
	v_cvt_scalef32_pk_fp8_f32 v115, v113, v114, s93
	v_med3_f32 v113, v161, -v255, v255
	v_med3_f32 v114, v165, -v255, v255
	v_cvt_scalef32_pk_fp8_f32 v116, v113, v114, s93
	v_med3_f32 v113, v162, -v255, v255
	v_med3_f32 v114, v166, -v255, v255
	s_bitcmp1_b32 s58, 0
	v_cvt_scalef32_pk_fp8_f32 v117, v113, v114, s93
	s_cselect_b32 s8, 0x1100, 0
	v_med3_f32 v113, v163, -v255, v255
	v_med3_f32 v114, v167, -v255, v255
	v_cmp_eq_u32_e32 vcc, 0, v181
	v_add_u32_e32 v112, s8, v195
	v_cvt_scalef32_pk_fp8_f32 v118, v113, v114, s93
	s_and_b64 vcc, exec, vcc
	s_and_b32 s24, s58, 31
	ds_write_b16 v112, v115
	ds_write_b16 v112, v116 offset:68
	ds_write_b16 v112, v117 offset:136
	ds_write_b16 v112, v118 offset:204
	s_cbranch_vccnz .LBB4_809
	s_lshl_b32 s8, s24, 7
	s_lshl_b32 s9, s58, 6
	s_and_b32 s8, s8, 0xf00
	s_and_b32 s9, s9, 64
	s_or_b32 s20, s8, s9
	s_cbranch_execnz .LBB4_803

; #define AT_SBAR() __builtin_amdgcn_sched_barrier(0)
; template <int D0> DI void pv_one(f32x16& od, int vb, bf16x8 pa0, bf16x8 pa1, bf16x8 pa2, bf16x8 pa3) {
;     const s16x4 l0 = tr_read<v_rd_off(D0, 0, 0)>(vb), h0 = tr_read<v_rd_off(D0, 0, 1)>(vb), l1 = tr_read<v_rd_off(D0, 1, 0)>(vb), h1 = tr_read<v_rd_off(D0, 1, 1)>(vb);
;     const s16x4 l2 = tr_read<v_rd_off(D0, 2, 0)>(vb), h2 = tr_read<v_rd_off(D0, 2, 1)>(vb), l3 = tr_read<v_rd_off(D0, 3, 0)>(vb), h3 = tr_read<v_rd_off(D0, 3, 1)>(vb);
;     asm volatile("s_waitcnt lgkmcnt(0)" ::: "memory"); AT_SBAR();
;     ...
;     od = __builtin_amdgcn_mfma_f32_32x32x16_bf16(AT_PK(l0, h0), pa0, od, 0, 0, 0);
;     od = __builtin_amdgcn_mfma_f32_32x32x16_bf16(AT_PK(l1, h1), pa1, od, 0, 0, 0);
;     od = __builtin_amdgcn_mfma_f32_32x32x16_bf16(AT_PK(l2, h2), pa2, od, 0, 0, 0);
;     od = __builtin_amdgcn_mfma_f32_32x32x16_bf16(AT_PK(l3, h3), pa3, od, 0, 0, 0);
;     ...
; }
; DI void pv_all_sm(f32x16* o, int vb, bf16x8 pa0, bf16x8 pa1, bf16x8 pa2, bf16x8 pa3, f32x16& p0, f32x16& p1, float& m_ref, f32x16& negm, float& alpha) {
;     pv_one<0>(o[0], vb, pa0, pa1, pa2, pa3);
;     float pmax = p0[0];
; #pragma unroll
;     for (int r = 1; r < 16; ++r) pmax = fmaxf(pmax, p0[r]);
;     pv_one<1>(o[1], vb, pa0, pa1, pa2, pa3);
; #pragma unroll
;     for (int r = 0; r < 16; ++r) pmax = fmaxf(pmax, p1[r]);
;     { auto rr = __builtin_amdgcn_permlane32_swap(__float_as_uint(pmax), __float_as_uint(pmax), false, false); pmax = fmaxf(__uint_as_float(rr[0]), __uint_as_float(rr[1])); }
;     pv_one<2>(o[2], vb, pa0, pa1, pa2, pa3);
;     alpha = 1.f;
;     if (__builtin_expect(!__all(pmax <= THRL), 0)) {
;         const float dl = fmaxf(pmax, 0.f); m_ref += dl; alpha = __builtin_amdgcn_exp2f(-dl);
; #pragma unroll
;         for (int r = 0; r < 16; ++r) { p0[r] -= dl; p1[r] -= dl; }
; #pragma unroll
;         for (int r = 0; r < 16; ++r) negm[r] = -m_ref;
;     }
;     pv_one<3>(o[3], vb, pa0, pa1, pa2, pa3);
; #pragma unroll
;     for (int r = 0; r < 16; ++r) p0[r] = __builtin_amdgcn_exp2f(p0[r]);
; }
; DI void attn_pass(const Frame& F, CvRide& cv, const bf16_t* __restrict__ Qb, const bf16_t* __restrict__ Kh, const bf16_t* __restrict__ Vh, char* lds, f32x16 (&o)[4], float& l_out, const int wave_s) {
;     ...
;     const unsigned cv_ldo = (unsigned)(((tid >> 4) * 2 * 2048 + (tid & 15) * 4) * 4), cv_sto = (unsigned)((tid >> 3) * 2048 + 8 * (tid & 7));
.LBB4_851:
	s_lshl_b32 s65, s63, 14
	v_add_u32_e32 v182, s65, v253
	ds_read_b64_tr_b16 v[64:65], v182 offset:0
	ds_read_b64_tr_b16 v[66:67], v182 offset:0x100
	ds_read_b64_tr_b16 v[68:69], v182 offset:0x1000
	ds_read_b64_tr_b16 v[70:71], v182 offset:0x1100
	ds_read_b64_tr_b16 v[72:73], v182 offset:0x2000
	ds_read_b64_tr_b16 v[74:75], v182 offset:0x2100
	ds_read_b64_tr_b16 v[76:77], v182 offset:0x3000
	ds_read_b64_tr_b16 v[78:79], v182 offset:0x3100
	s_waitcnt lgkmcnt(0)
	v_mfma_f32_32x32x16_bf16 v[32:47], v[64:67], v[96:99], v[32:47]
	v_max_f32_e32 v64, v128, v129
	v_max3_f32 v64, v64, v130, v131
	v_max3_f32 v64, v64, v132, v133
	v_max3_f32 v64, v64, v134, v135
	v_max3_f32 v64, v64, v136, v137
	v_mfma_f32_32x32x16_bf16 v[32:47], v[68:71], v[108:111], v[32:47]
	v_max3_f32 v64, v64, v138, v139
	v_max3_f32 v66, v64, v140, v141
	ds_read_b64_tr_b16 v[64:65], v182 offset:0x200
	v_max3_f32 v180, v66, v142, v143
	ds_read_b64_tr_b16 v[66:67], v182 offset:0x300
	ds_read_b64_tr_b16 v[68:69], v182 offset:0x1200
	ds_read_b64_tr_b16 v[70:71], v182 offset:0x1300
	v_mfma_f32_32x32x16_bf16 v[32:47], v[72:75], v[100:103], v[32:47]
	ds_read_b64_tr_b16 v[72:73], v182 offset:0x2200
	ds_read_b64_tr_b16 v[74:75], v182 offset:0x2300
	ds_read_b64_tr_b16 v[214:215], v182 offset:0x3200
	ds_read_b64_tr_b16 v[216:217], v182 offset:0x3300
	v_mfma_f32_32x32x16_bf16 v[32:47], v[76:79], v[104:107], v[32:47]
	s_waitcnt lgkmcnt(0)
	v_mfma_f32_32x32x16_bf16 v[48:63], v[64:67], v[96:99], v[48:63]
	v_max3_f32 v76, v180, v112, v113
	v_max3_f32 v64, v76, v114, v115
	ds_read_b64_tr_b16 v[66:67], v182 offset:0x400
	v_max3_f32 v64, v64, v116, v117
	v_max3_f32 v64, v64, v118, v119
	v_max3_f32 v64, v64, v120, v121
	v_max3_f32 v64, v64, v122, v123
	v_mfma_f32_32x32x16_bf16 v[48:63], v[68:71], v[108:111], v[48:63]
	ds_read_b64_tr_b16 v[68:69], v182 offset:0x500
	ds_read_b64_tr_b16 v[70:71], v182 offset:0x1400
	v_max3_f32 v64, v64, v124, v125
	v_max3_f32 v64, v64, v126, v127
	v_mov_b32_e32 v65, v64
	s_nop 1
	v_permlane32_swap_b32_e32 v64, v65
	v_mfma_f32_32x32x16_bf16 v[48:63], v[72:75], v[100:103], v[48:63]
	ds_read_b64_tr_b16 v[72:73], v182 offset:0x1500
	ds_read_b64_tr_b16 v[74:75], v182 offset:0x2400
	ds_read_b64_tr_b16 v[76:77], v182 offset:0x2500
	ds_read_b64_tr_b16 v[218:219], v182 offset:0x3400
	ds_read_b64_tr_b16 v[220:221], v182 offset:0x3500
	v_mfma_f32_32x32x16_bf16 v[48:63], v[214:217], v[104:107], v[48:63]
	s_waitcnt lgkmcnt(0)
	v_max_f32_e32 v64, v64, v65
	v_mfma_f32_32x32x16_bf16 v[16:31], v[66:69], v[96:99], v[16:31]
	v_cmp_ge_f32_e32 vcc, s15, v64
	s_cmp_eq_u64 vcc, exec
	v_mfma_f32_32x32x16_bf16 v[16:31], v[70:73], v[108:111], v[16:31]
	v_mfma_f32_32x32x16_bf16 v[16:31], v[74:77], v[100:103], v[16:31]
	v_mfma_f32_32x32x16_bf16 v[16:31], v[218:221], v[104:107], v[16:31]
	s_cbranch_scc0 .LBB4_884
	v_mov_b32_e32 v180, 1.0
.LBB4_853:
	ds_read_b64_tr_b16 v[214:215], v182 offset:0x600
	ds_read_b64_tr_b16 v[216:217], v182 offset:0x700
	ds_read_b64_tr_b16 v[218:219], v182 offset:0x1600
	ds_read_b64_tr_b16 v[220:221], v182 offset:0x1700
	ds_read_b64_tr_b16 v[222:223], v182 offset:0x2600
	ds_read_b64_tr_b16 v[224:225], v182 offset:0x2700
	ds_read_b64_tr_b16 v[226:227], v182 offset:0x3600
	ds_read_b64_tr_b16 v[228:229], v182 offset:0x3700
	s_waitcnt lgkmcnt(0)
	v_mfma_f32_32x32x16_bf16 v[0:15], v[214:217], v[96:99], v[0:15]
	s_lshl_b32 s2, s57, 14
	s_add_i32 s2, s2, 0
	s_lshl_b32 s3, s57, 13
	v_add_u32_e32 v96, s2, v199
	s_sub_i32 s76, s2, s3
	s_waitcnt vmcnt(0)
	v_add_u32_e32 v97, s2, v200
	v_mfma_f32_32x32x16_bf16 v[0:15], v[218:221], v[108:111], v[0:15]
	ds_write_b128 v96, v[176:179]
	v_add_u32_e32 v96, s76, v201
	ds_write_b128 v97, v[172:175]
	ds_write_b128 v96, v[168:171] offset:49152
	s_andn2_b64 s[2:3], exec, s[30:31]
	s_andn2_b64 vcc, exec, s[30:31]
	v_mfma_f32_32x32x16_bf16 v[0:15], v[222:225], v[100:103], v[0:15]
	v_mfma_f32_32x32x16_bf16 v[0:15], v[226:229], v[104:107], v[0:15]
	s_cbranch_vccnz .LBB4_858
	v_med3_f32 v97, v160, -v255, v255
	v_med3_f32 v98, v164, -v255, v255
	v_cvt_scalef32_pk_fp8_f32 v99, v97, v98, s93
	v_med3_f32 v97, v161, -v255, v255
	v_med3_f32 v98, v165, -v255, v255
	v_cvt_scalef32_pk_fp8_f32 v100, v97, v98, s93
	v_med3_f32 v97, v162, -v255, v255
	v_med3_f32 v98, v166, -v255, v255
	s_bitcmp1_b32 s58, 0
	v_cvt_scalef32_pk_fp8_f32 v101, v97, v98, s93
	s_cselect_b32 s8, 0x1100, 0
	v_med3_f32 v97, v163, -v255, v255
	v_med3_f32 v98, v167, -v255, v255
	v_cmp_eq_u32_e32 vcc, 0, v181
	v_add_u32_e32 v96, s8, v190
	v_cvt_scalef32_pk_fp8_f32 v102, v97, v98, s93
	s_and_b64 vcc, exec, vcc
	s_and_b32 s30, s58, 31
	ds_write_b16 v96, v99
	ds_write_b16 v96, v100 offset:68
	ds_write_b16 v96, v101 offset:136
	ds_write_b16 v96, v102 offset:204
	s_cbranch_vccnz .LBB4_882
	s_lshl_b32 s8, s30, 7
	s_lshl_b32 s9, s58, 6
	s_and_b32 s8, s8, 0xf00
	s_and_b32 s9, s9, 64
	s_or_b32 s26, s8, s9
	s_cbranch_execnz .LBB4_857

; #define AT_SBAR() __builtin_amdgcn_sched_barrier(0)
; template <int D0> DI void pv_one(f32x16& od, int vb, bf16x8 pa0, bf16x8 pa1, bf16x8 pa2, bf16x8 pa3) {
;     const s16x4 l0 = tr_read<v_rd_off(D0, 0, 0)>(vb), h0 = tr_read<v_rd_off(D0, 0, 1)>(vb), l1 = tr_read<v_rd_off(D0, 1, 0)>(vb), h1 = tr_read<v_rd_off(D0, 1, 1)>(vb);
;     const s16x4 l2 = tr_read<v_rd_off(D0, 2, 0)>(vb), h2 = tr_read<v_rd_off(D0, 2, 1)>(vb), l3 = tr_read<v_rd_off(D0, 3, 0)>(vb), h3 = tr_read<v_rd_off(D0, 3, 1)>(vb);
;     asm volatile("s_waitcnt lgkmcnt(0)" ::: "memory"); AT_SBAR();
;     ...
;     od = __builtin_amdgcn_mfma_f32_32x32x16_bf16(AT_PK(l0, h0), pa0, od, 0, 0, 0);
;     od = __builtin_amdgcn_mfma_f32_32x32x16_bf16(AT_PK(l1, h1), pa1, od, 0, 0, 0);
;     od = __builtin_amdgcn_mfma_f32_32x32x16_bf16(AT_PK(l2, h2), pa2, od, 0, 0, 0);
;     od = __builtin_amdgcn_mfma_f32_32x32x16_bf16(AT_PK(l3, h3), pa3, od, 0, 0, 0);
;     ...
; }
; DI void pv_all_sm(f32x16* o, int vb, bf16x8 pa0, bf16x8 pa1, bf16x8 pa2, bf16x8 pa3, f32x16& p0, f32x16& p1, float& m_ref, f32x16& negm, float& alpha) {
;     pv_one<0>(o[0], vb, pa0, pa1, pa2, pa3);
;     float pmax = p0[0];
; #pragma unroll
;     for (int r = 1; r < 16; ++r) pmax = fmaxf(pmax, p0[r]);
;     pv_one<1>(o[1], vb, pa0, pa1, pa2, pa3);
; #pragma unroll
;     for (int r = 0; r < 16; ++r) pmax = fmaxf(pmax, p1[r]);
;     { auto rr = __builtin_amdgcn_permlane32_swap(__float_as_uint(pmax), __float_as_uint(pmax), false, false); pmax = fmaxf(__uint_as_float(rr[0]), __uint_as_float(rr[1])); }
;     pv_one<2>(o[2], vb, pa0, pa1, pa2, pa3);
;     alpha = 1.f;
;     if (__builtin_expect(!__all(pmax <= THRL), 0)) {
;         const float dl = fmaxf(pmax, 0.f); m_ref += dl; alpha = __builtin_amdgcn_exp2f(-dl);
; #pragma unroll
;         for (int r = 0; r < 16; ++r) { p0[r] -= dl; p1[r] -= dl; }
; #pragma unroll
;         for (int r = 0; r < 16; ++r) negm[r] = -m_ref;
;     }
;     pv_one<3>(o[3], vb, pa0, pa1, pa2, pa3);
; #pragma unroll
;     for (int r = 0; r < 16; ++r) p0[r] = __builtin_amdgcn_exp2f(p0[r]);
; }
; DI void attn_pass(const Frame& F, CvRide& cv, const bf16_t* __restrict__ Qb, const bf16_t* __restrict__ Kh, const bf16_t* __restrict__ Vh, char* lds, f32x16 (&o)[4], float& l_out, const int wave_s) {
;     ...
;     const unsigned cv_ldo = (unsigned)(((tid >> 4) * 2 * 2048 + (tid & 15) * 4) * 4), cv_sto = (unsigned)((tid >> 3) * 2048 + 8 * (tid & 7));
.LBB4_872:
	v_lshl_add_u32 v215, s64, 14, v253
	ds_read_b64_tr_b16 v[216:217], v215 offset:0
	ds_read_b64_tr_b16 v[218:219], v215 offset:0x100
	ds_read_b64_tr_b16 v[220:221], v215 offset:0x1000
	ds_read_b64_tr_b16 v[222:223], v215 offset:0x1100
	ds_read_b64_tr_b16 v[224:225], v215 offset:0x2000
	ds_read_b64_tr_b16 v[226:227], v215 offset:0x2100
	ds_read_b64_tr_b16 v[228:229], v215 offset:0x3000
	ds_read_b64_tr_b16 v[230:231], v215 offset:0x3100
	s_waitcnt lgkmcnt(0)
	v_mfma_f32_32x32x16_bf16 v[32:47], v[216:219], v[120:123], v[32:47]
	v_max_f32_e32 v182, v128, v129
	ds_read_b64_tr_b16 v[216:217], v215 offset:0x200
	ds_read_b64_tr_b16 v[218:219], v215 offset:0x300
	v_max3_f32 v182, v182, v130, v131
	v_max3_f32 v182, v182, v132, v133
	v_mfma_f32_32x32x16_bf16 v[32:47], v[220:223], v[124:127], v[32:47]
	ds_read_b64_tr_b16 v[220:221], v215 offset:0x1200
	ds_read_b64_tr_b16 v[222:223], v215 offset:0x1300
	v_max3_f32 v182, v182, v134, v135
	v_max3_f32 v182, v182, v136, v137
	v_max3_f32 v182, v182, v138, v139
	v_max3_f32 v182, v182, v140, v141
	v_max3_f32 v182, v182, v142, v143
	v_mfma_f32_32x32x16_bf16 v[32:47], v[224:227], v[112:115], v[32:47]
	ds_read_b64_tr_b16 v[224:225], v215 offset:0x2200
	ds_read_b64_tr_b16 v[226:227], v215 offset:0x2300
	ds_read_b64_tr_b16 v[232:233], v215 offset:0x3200
	ds_read_b64_tr_b16 v[234:235], v215 offset:0x3300
	v_mfma_f32_32x32x16_bf16 v[32:47], v[228:231], v[116:119], v[32:47]
	s_waitcnt lgkmcnt(0)
	v_mfma_f32_32x32x16_bf16 v[48:63], v[216:219], v[120:123], v[48:63]
	v_max3_f32 v182, v182, v96, v97
	v_max3_f32 v182, v182, v98, v99
	ds_read_b64_tr_b16 v[218:219], v215 offset:0x400
	v_max3_f32 v182, v182, v100, v101
	v_max3_f32 v182, v182, v102, v103
	v_max3_f32 v182, v182, v104, v105
	v_max3_f32 v182, v182, v106, v107
	v_mfma_f32_32x32x16_bf16 v[48:63], v[220:223], v[124:127], v[48:63]
	ds_read_b64_tr_b16 v[220:221], v215 offset:0x500
	ds_read_b64_tr_b16 v[222:223], v215 offset:0x1400
	v_max3_f32 v182, v182, v108, v109
	v_max3_f32 v182, v182, v110, v111
	v_mov_b32_e32 v216, v182
	s_nop 1
	v_permlane32_swap_b32_e32 v182, v216
	v_mfma_f32_32x32x16_bf16 v[48:63], v[224:227], v[112:115], v[48:63]
	ds_read_b64_tr_b16 v[224:225], v215 offset:0x1500
	ds_read_b64_tr_b16 v[226:227], v215 offset:0x2400
	ds_read_b64_tr_b16 v[228:229], v215 offset:0x2500
	ds_read_b64_tr_b16 v[236:237], v215 offset:0x3400
	ds_read_b64_tr_b16 v[238:239], v215 offset:0x3500
	v_mfma_f32_32x32x16_bf16 v[48:63], v[232:235], v[116:119], v[48:63]
	s_waitcnt lgkmcnt(0)
	v_max_f32_e32 v216, v182, v216
	v_mfma_f32_32x32x16_bf16 v[16:31], v[218:221], v[120:123], v[16:31]
	v_cmp_ge_f32_e32 vcc, s15, v216
	s_cmp_eq_u64 vcc, exec
	v_mov_b32_e32 v182, 1.0
	v_mfma_f32_32x32x16_bf16 v[16:31], v[222:225], v[124:127], v[16:31]
	v_mfma_f32_32x32x16_bf16 v[16:31], v[226:229], v[112:115], v[16:31]
	v_mfma_f32_32x32x16_bf16 v[16:31], v[236:239], v[116:119], v[16:31]
	s_cbranch_scc0 .LBB4_885
.LBB4_873:
	ds_read_b64_tr_b16 v[216:217], v215 offset:0x600
	ds_read_b64_tr_b16 v[218:219], v215 offset:0x700
	ds_read_b64_tr_b16 v[220:221], v215 offset:0x1600
	ds_read_b64_tr_b16 v[222:223], v215 offset:0x1700
	ds_read_b64_tr_b16 v[224:225], v215 offset:0x2600
	ds_read_b64_tr_b16 v[226:227], v215 offset:0x2700
	ds_read_b64_tr_b16 v[228:229], v215 offset:0x3600
	ds_read_b64_tr_b16 v[230:231], v215 offset:0x3700
	s_waitcnt lgkmcnt(0)
	v_mfma_f32_32x32x16_bf16 v[0:15], v[216:219], v[120:123], v[0:15]
	s_add_i32 s2, s65, 0
	v_add_u32_e32 v120, s2, v199
	s_waitcnt vmcnt(0)
	ds_write_b128 v120, v[176:179]
	s_mov_b32 s26, 0
	s_andn2_b64 vcc, exec, s[30:31]
	v_mfma_f32_32x32x16_bf16 v[0:15], v[220:223], v[124:127], v[0:15]
	v_mfma_f32_32x32x16_bf16 v[0:15], v[224:227], v[112:115], v[0:15]
	v_add_u32_e32 v112, s2, v200
	ds_write_b128 v112, v[172:175]
	v_lshl_add_u32 v112, s63, 13, v202
	ds_write_b128 v112, v[168:171] offset:49152
	s_andn2_b64 s[2:3], exec, s[30:31]
	v_mfma_f32_32x32x16_bf16 v[0:15], v[228:231], v[116:119], v[0:15]
	s_cbranch_vccnz .LBB4_878
	v_med3_f32 v113, v160, -v255, v255
	v_med3_f32 v114, v164, -v255, v255
	v_cvt_scalef32_pk_fp8_f32 v115, v113, v114, s93
	v_med3_f32 v113, v161, -v255, v255
	v_med3_f32 v114, v165, -v255, v255
	v_cvt_scalef32_pk_fp8_f32 v116, v113, v114, s93
	v_med3_f32 v113, v162, -v255, v255
	v_med3_f32 v114, v166, -v255, v255
	s_bitcmp1_b32 s58, 0
	v_cvt_scalef32_pk_fp8_f32 v117, v113, v114, s93
	s_cselect_b32 s8, 0x1100, 0
	v_med3_f32 v113, v163, -v255, v255
	v_med3_f32 v114, v167, -v255, v255
	v_cmp_eq_u32_e32 vcc, 0, v181
	v_add_u32_e32 v112, s8, v190
	v_cvt_scalef32_pk_fp8_f32 v118, v113, v114, s93
	s_and_b64 vcc, exec, vcc
	s_and_b32 s34, s58, 31
	ds_write_b16 v112, v115
	ds_write_b16 v112, v116 offset:68
	ds_write_b16 v112, v117 offset:136
	ds_write_b16 v112, v118 offset:204
	s_cbranch_vccnz .LBB4_883
	s_lshl_b32 s8, s34, 7
	s_lshl_b32 s9, s58, 6
	s_and_b32 s8, s8, 0xf00
	s_and_b32 s9, s9, 64
	s_or_b32 s26, s8, s9
	s_cbranch_execnz .LBB4_877

; #define AT_SBAR() __builtin_amdgcn_sched_barrier(0)
; template <int OFF> DI s16x4 tr_read(int vb) { s16x4 r; asm volatile("ds_read_b64_tr_b16 %0, %1 offset:%2" : "=&v"(r) : "v"(vb), "i"(OFF) : "memory"); return r; }
; template <int D0> DI void pv_one(f32x16& od, int vb, bf16x8 pa0, bf16x8 pa1, bf16x8 pa2, bf16x8 pa3) {
;     const s16x4 l0 = tr_read<v_rd_off(D0, 0, 0)>(vb), h0 = tr_read<v_rd_off(D0, 0, 1)>(vb), l1 = tr_read<v_rd_off(D0, 1, 0)>(vb), h1 = tr_read<v_rd_off(D0, 1, 1)>(vb);
;     const s16x4 l2 = tr_read<v_rd_off(D0, 2, 0)>(vb), h2 = tr_read<v_rd_off(D0, 2, 1)>(vb), l3 = tr_read<v_rd_off(D0, 3, 0)>(vb), h3 = tr_read<v_rd_off(D0, 3, 1)>(vb);
;     asm volatile("s_waitcnt lgkmcnt(0)" ::: "memory"); AT_SBAR();
;     ...
;     od = __builtin_amdgcn_mfma_f32_32x32x16_bf16(AT_PK(l0, h0), pa0, od, 0, 0, 0);
;     od = __builtin_amdgcn_mfma_f32_32x32x16_bf16(AT_PK(l1, h1), pa1, od, 0, 0, 0);
;     od = __builtin_amdgcn_mfma_f32_32x32x16_bf16(AT_PK(l2, h2), pa2, od, 0, 0, 0);
;     od = __builtin_amdgcn_mfma_f32_32x32x16_bf16(AT_PK(l3, h3), pa3, od, 0, 0, 0);
; DI void attn_pass(const Frame& F, CvRide& cv, const bf16_t* __restrict__ Qb, const bf16_t* __restrict__ Kh, const bf16_t* __restrict__ Vh, char* lds, f32x16 (&o)[4], float& l_out, const int wave_s) {
;     ...
;     const unsigned cv_ldo = (unsigned)(((tid >> 4) * 2 * 2048 + (tid & 15) * 4) * 4), cv_sto = (unsigned)((tid >> 3) * 2048 + 8 * (tid & 7));
;     const int cv_lw = OFF_CV + (4 * (tid & 15)) * 68 + 2 * (tid >> 4), cv_lr = OFF_CV + (tid >> 3) * 68 + 8 * (tid & 7);
;     f32x4 cvA = f32x4{}, cvB = f32x4{}; unsigned cvr0 = 0, cvr1 = 0;
.LBB4_927:
	ds_read_b64_tr_b16 v[218:219], v182 offset:0x600
	ds_read_b64_tr_b16 v[220:221], v182 offset:0x700
	ds_read_b64_tr_b16 v[222:223], v182 offset:0x1600
	ds_read_b64_tr_b16 v[224:225], v182 offset:0x1700
	ds_read_b64_tr_b16 v[226:227], v182 offset:0x2600
	ds_read_b64_tr_b16 v[228:229], v182 offset:0x2700
	ds_read_b64_tr_b16 v[230:231], v182 offset:0x3600
	ds_read_b64_tr_b16 v[232:233], v182 offset:0x3700
	s_waitcnt lgkmcnt(0)
	v_mfma_f32_32x32x16_bf16 v[0:15], v[218:221], v[96:99], v[0:15]
	s_lshl_b32 s2, s15, 14
	s_add_i32 s2, s2, 0
	s_lshl_b32 s3, s15, 13
	v_add_u32_e32 v96, s2, v203
	s_sub_i32 s54, s2, s3
	s_waitcnt vmcnt(0)
	v_add_u32_e32 v97, s2, v204
	v_mfma_f32_32x32x16_bf16 v[0:15], v[222:225], v[108:111], v[0:15]
	ds_write_b128 v96, v[176:179]
	v_add_u32_e32 v96, s54, v205
	ds_write_b128 v97, v[172:175]
	ds_write_b128 v96, v[168:171] offset:49152
	s_andn2_b64 s[2:3], exec, s[22:23]
	s_andn2_b64 vcc, exec, s[22:23]
	v_mfma_f32_32x32x16_bf16 v[0:15], v[226:229], v[100:103], v[0:15]
	v_mfma_f32_32x32x16_bf16 v[0:15], v[230:233], v[104:107], v[0:15]
	s_cbranch_vccnz .LBB4_932
	v_med3_f32 v97, v160, -v255, v255
	v_med3_f32 v98, v164, -v255, v255
	v_cvt_scalef32_pk_fp8_f32 v99, v97, v98, s93
	v_med3_f32 v97, v161, -v255, v255
	v_med3_f32 v98, v165, -v255, v255
	v_cvt_scalef32_pk_fp8_f32 v100, v97, v98, s93
	v_med3_f32 v97, v162, -v255, v255
	v_med3_f32 v98, v166, -v255, v255
	s_bitcmp1_b32 s58, 0
	v_cvt_scalef32_pk_fp8_f32 v101, v97, v98, s93
	s_cselect_b32 s8, 0x1100, 0
	v_med3_f32 v97, v163, -v255, v255
	v_med3_f32 v98, v167, -v255, v255
	v_cmp_eq_u32_e32 vcc, 0, v181
	v_add_u32_e32 v96, s8, v195
	v_cvt_scalef32_pk_fp8_f32 v102, v97, v98, s93
	s_and_b64 vcc, exec, vcc
	s_and_b32 s22, s58, 31
	ds_write_b16 v96, v99
	ds_write_b16 v96, v100 offset:68
	ds_write_b16 v96, v101 offset:136
	ds_write_b16 v96, v102 offset:204
	s_cbranch_vccnz .LBB4_956
	s_lshl_b32 s8, s22, 7
	s_lshl_b32 s9, s58, 6
	s_and_b32 s8, s8, 0xf00
	s_and_b32 s9, s9, 64
	s_or_b32 s18, s8, s9
	s_cbranch_execnz .LBB4_931

; #define AT_SBAR() __builtin_amdgcn_sched_barrier(0)
; template <int OFF> DI s16x4 tr_read(int vb) { s16x4 r; asm volatile("ds_read_b64_tr_b16 %0, %1 offset:%2" : "=&v"(r) : "v"(vb), "i"(OFF) : "memory"); return r; }
; template <int D0> DI void pv_one(f32x16& od, int vb, bf16x8 pa0, bf16x8 pa1, bf16x8 pa2, bf16x8 pa3) {
;     const s16x4 l0 = tr_read<v_rd_off(D0, 0, 0)>(vb), h0 = tr_read<v_rd_off(D0, 0, 1)>(vb), l1 = tr_read<v_rd_off(D0, 1, 0)>(vb), h1 = tr_read<v_rd_off(D0, 1, 1)>(vb);
;     const s16x4 l2 = tr_read<v_rd_off(D0, 2, 0)>(vb), h2 = tr_read<v_rd_off(D0, 2, 1)>(vb), l3 = tr_read<v_rd_off(D0, 3, 0)>(vb), h3 = tr_read<v_rd_off(D0, 3, 1)>(vb);
;     asm volatile("s_waitcnt lgkmcnt(0)" ::: "memory"); AT_SBAR();
;     ...
;     od = __builtin_amdgcn_mfma_f32_32x32x16_bf16(AT_PK(l0, h0), pa0, od, 0, 0, 0);
;     od = __builtin_amdgcn_mfma_f32_32x32x16_bf16(AT_PK(l1, h1), pa1, od, 0, 0, 0);
;     od = __builtin_amdgcn_mfma_f32_32x32x16_bf16(AT_PK(l2, h2), pa2, od, 0, 0, 0);
;     od = __builtin_amdgcn_mfma_f32_32x32x16_bf16(AT_PK(l3, h3), pa3, od, 0, 0, 0);
; DI void attn_pass(const Frame& F, CvRide& cv, const bf16_t* __restrict__ Qb, const bf16_t* __restrict__ Kh, const bf16_t* __restrict__ Vh, char* lds, f32x16 (&o)[4], float& l_out, const int wave_s) {
;     ...
;     const unsigned cv_ldo = (unsigned)(((tid >> 4) * 2 * 2048 + (tid & 15) * 4) * 4), cv_sto = (unsigned)((tid >> 3) * 2048 + 8 * (tid & 7));
;     const int cv_lw = OFF_CV + (4 * (tid & 15)) * 68 + 2 * (tid >> 4), cv_lr = OFF_CV + (tid >> 3) * 68 + 8 * (tid & 7);
;     f32x4 cvA = f32x4{}, cvB = f32x4{}; unsigned cvr0 = 0, cvr1 = 0;
.LBB4_947:
	ds_read_b64_tr_b16 v[220:221], v219 offset:0x600
	ds_read_b64_tr_b16 v[222:223], v219 offset:0x700
	ds_read_b64_tr_b16 v[224:225], v219 offset:0x1600
	ds_read_b64_tr_b16 v[226:227], v219 offset:0x1700
	ds_read_b64_tr_b16 v[228:229], v219 offset:0x2600
	ds_read_b64_tr_b16 v[230:231], v219 offset:0x2700
	ds_read_b64_tr_b16 v[232:233], v219 offset:0x3600
	ds_read_b64_tr_b16 v[234:235], v219 offset:0x3700
	s_waitcnt lgkmcnt(0)
	v_mfma_f32_32x32x16_bf16 v[0:15], v[220:223], v[120:123], v[0:15]
	s_add_i32 s2, s31, 0
	v_add_u32_e32 v120, s2, v203
	s_waitcnt vmcnt(0)
	ds_write_b128 v120, v[176:179]
	s_mov_b32 s18, 0
	s_andn2_b64 vcc, exec, s[22:23]
	v_mfma_f32_32x32x16_bf16 v[0:15], v[224:227], v[124:127], v[0:15]
	v_mfma_f32_32x32x16_bf16 v[0:15], v[228:231], v[112:115], v[0:15]
	v_add_u32_e32 v112, s2, v204
	ds_write_b128 v112, v[172:175]
	v_lshl_add_u32 v112, s29, 13, v206
	ds_write_b128 v112, v[168:171] offset:49152
	s_andn2_b64 s[2:3], exec, s[22:23]
	v_mfma_f32_32x32x16_bf16 v[0:15], v[232:235], v[116:119], v[0:15]
	s_cbranch_vccnz .LBB4_952
	v_med3_f32 v113, v160, -v255, v255
	v_med3_f32 v114, v164, -v255, v255
	v_cvt_scalef32_pk_fp8_f32 v115, v113, v114, s93
	v_med3_f32 v113, v161, -v255, v255
	v_med3_f32 v114, v165, -v255, v255
	v_cvt_scalef32_pk_fp8_f32 v116, v113, v114, s93
	v_med3_f32 v113, v162, -v255, v255
	v_med3_f32 v114, v166, -v255, v255
	s_bitcmp1_b32 s58, 0
	v_cvt_scalef32_pk_fp8_f32 v117, v113, v114, s93
	s_cselect_b32 s8, 0x1100, 0
	v_med3_f32 v113, v163, -v255, v255
	v_med3_f32 v114, v167, -v255, v255
	v_cmp_eq_u32_e32 vcc, 0, v181
	v_add_u32_e32 v112, s8, v195
	v_cvt_scalef32_pk_fp8_f32 v118, v113, v114, s93
	s_and_b64 vcc, exec, vcc
	s_and_b32 s24, s58, 31
	ds_write_b16 v112, v115
	ds_write_b16 v112, v116 offset:68
	ds_write_b16 v112, v117 offset:136
	ds_write_b16 v112, v118 offset:204
	s_cbranch_vccnz .LBB4_957
	s_lshl_b32 s8, s24, 7
	s_lshl_b32 s9, s58, 6
	s_and_b32 s8, s8, 0xf00
	s_and_b32 s9, s9, 64
	s_or_b32 s18, s8, s9
	s_cbranch_execnz .LBB4_951
